# v9: DPP wave reductions in quant/gather passes, residual epilogues issue both halves' loads together
# baseline (speedup 1.0000x reference)
; __device__ __forceinline__ u64_t* ssq_ptr(unsigned char* ws, int v) { return (u64_t*)(ws + CTL_SSQ) + (size_t)v * NTOK; }
; __device__ __forceinline__ u64_t ssq_fix(float ss) { return (u64_t)(ss * 16777216.0f); }
; #define ROW_FENCE() asm volatile("" ::: "memory")
; __device__ __forceinline__ u32x4 pack8(const f32x4& a, const f32x4& b) { u32x4 w; w.x = pk_bf16(a[0], a[1]); w.y = pk_bf16(a[2], a[3]); w.z = pk_bf16(b[0], b[1]); w.w = pk_bf16(b[2], b[3]); return w; }
;     __device__ __forceinline__ void operator()(const f32x4 (&acc)[2][2][4][2], const pg8::Unit& u, int wr, int wc, int fr, int fq) const {
;         bf16_t* xb = (bf16_t*)(ws + WS_XB); u64_t* ssq = ssq_ptr(ws, v);
;         float osc = 1.0f; if constexpr (SC) osc = __uint_as_float(((const unsigned*)(ws + CTL_AMAX))[AMAX_W2]) * (1.0f / 256.0f);
;         const int col = u.pn * 256 + wc * 32 + 8 * fq;
; #pragma unroll
;         for (int ai = 0; ai < 2; ++ai) {
;             u32x4 bs[4][2];
; #pragma unroll
;             for (int m = 0; m < 4; ++m) { const size_t off = (size_t)(u.pm * 256 + ai * 128 + wr * 64 + m * 16 + fr) * D + col;
; #pragma unroll
;                 for (int bj = 0; bj < 2; ++bj) bs[m][bj] = *(const u32x4*)(xb + off + bj * 128); }
;             ROW_FENCE();
; #pragma unroll
;             for (int m = 0; m < 4; ++m) {
;                 const int row = u.pm * 256 + ai * 128 + wr * 64 + m * 16 + fr; const size_t off = (size_t)row * D + col; float ss = 0.f;
;                 float rsc = osc; if constexpr (SC) asm volatile("" : "+v"(rsc));
; #pragma unroll
;                 for (int bj = 0; bj < 2; ++bj) { f32x4 b0, b1; unpack8(bs[m][bj], b0, b1); const f32x4 x0 = SC ? b0 + acc[ai][bj][m][0] * rsc : b0 + acc[ai][bj][m][0], x1 = SC ? b1 + acc[ai][bj][m][1] * rsc : b1 + acc[ai][bj][m][1];
;                     if (!dry) *(u32x4*)(xb + off + bj * 128) = pack8(x0, x1);
;                     ss += ((x0[0] * x0[0] + x0[1] * x0[1]) + (x0[2] * x0[2] + x0[3] * x0[3])) + ((x1[0] * x1[0] + x1[1] * x1[1]) + (x1[2] * x1[2] + x1[3] * x1[3])); }
;                 ss += __shfl_xor(ss, 16); ss += __shfl_xor(ss, 32);
;                 if (fq == 0 && !dry) atomicAdd(ssq + row, ssq_fix(ss));
;             }
.LBB0_1089:
	s_mov_b32 s11, s93
	v_and_b32_e32 v170, 64, v251
	v_mbcnt_lo_u32_b32 v130, -1, s11
	v_mbcnt_hi_u32_b32 v171, -1, v130
	s_lshl_b32 s11, s45, 8
	v_ashrrev_i32_e32 v130, 1, v171
	s_or_b32 s11, s11, s40
	v_and_b32_e32 v130, -8, v130
	v_add_u32_e32 v130, s11, v130
	s_lshl_b32 s11, s18, 8
	s_add_i32 s11, s11, s39
	v_and_or_b32 v156, v171, 15, s11
	v_ashrrev_i32_e32 v131, 31, v130
	v_ashrrev_i32_e32 v157, 31, v156
	v_lshl_add_u64 v[158:159], v[130:131], 1, s[6:7]
	v_lshlrev_b64 v[130:131], 11, v[156:157]
	v_lshl_add_u64 v[180:181], v[158:159], 0, v[130:131]
	flat_load_dwordx4 v[172:175], v[180:181]
	flat_load_dwordx4 v[176:179], v[180:181] offset:256
	v_or_b32_e32 v130, 16, v156
	v_or_b32_e32 v132, 32, v156
	v_or_b32_e32 v134, 48, v156
	v_ashrrev_i32_e32 v131, 31, v130
	v_ashrrev_i32_e32 v133, 31, v132
	v_ashrrev_i32_e32 v135, 31, v134
	v_lshlrev_b64 v[130:131], 11, v[130:131]
	v_lshlrev_b64 v[132:133], 11, v[132:133]
	v_lshlrev_b64 v[134:135], 11, v[134:135]
	v_lshl_add_u64 v[168:169], v[158:159], 0, v[130:131]
	v_lshl_add_u64 v[162:163], v[158:159], 0, v[132:133]
	v_lshl_add_u64 v[160:161], v[158:159], 0, v[134:135]
	flat_load_dwordx4 v[150:153], v[168:169]
	flat_load_dwordx4 v[146:149], v[168:169] offset:256
	flat_load_dwordx4 v[142:145], v[162:163]
	flat_load_dwordx4 v[138:141], v[162:163] offset:256
	flat_load_dwordx4 v[134:137], v[160:161]
	flat_load_dwordx4 v[130:133], v[160:161] offset:256
	v_mov_b32_e32 v246, 0x40000
	v_mov_b32_e32 v247, 0
	v_lshl_add_u64 v[238:239], v[180:181], 0, v[246:247]
	v_lshl_add_u64 v[240:241], v[168:169], 0, v[246:247]
	v_lshl_add_u64 v[242:243], v[162:163], 0, v[246:247]
	v_lshl_add_u64 v[244:245], v[160:161], 0, v[246:247]
	flat_load_dwordx4 v[206:209], v[238:239]
	flat_load_dwordx4 v[210:213], v[238:239] offset:256
	flat_load_dwordx4 v[214:217], v[240:241]
	flat_load_dwordx4 v[218:221], v[240:241] offset:256
	flat_load_dwordx4 v[222:225], v[242:243]
	flat_load_dwordx4 v[226:229], v[242:243] offset:256
	flat_load_dwordx4 v[230:233], v[244:245]
	flat_load_dwordx4 v[234:237], v[244:245] offset:256
	v_xor_b32_e32 v167, 16, v251
	v_add_u32_e32 v170, 64, v170
	v_xor_b32_e32 v182, 32, v251
	v_cmp_lt_i32_e32 vcc, v167, v170
	s_waitcnt vmcnt(0) lgkmcnt(0)
	v_and_b32_e32 v183, 0xffff0000, v172
	v_cndmask_b32_e32 v167, v251, v167, vcc
	v_cmp_lt_i32_e32 vcc, v182, v170
	v_lshlrev_b32_e32 v170, 2, v167
	v_lshlrev_b32_e32 v184, 16, v174
	v_cndmask_b32_e32 v182, v251, v182, vcc
	v_lshlrev_b32_e32 v167, 2, v182
	v_lshlrev_b32_e32 v182, 16, v172
	v_lshlrev_b32_e32 v172, 16, v173
	v_and_b32_e32 v173, 0xffff0000, v173
	v_and_b32_e32 v185, 0xffff0000, v174
	v_lshlrev_b32_e32 v174, 16, v175
	v_and_b32_e32 v175, 0xffff0000, v175
	v_lshlrev_b32_e32 v186, 16, v176
	v_and_b32_e32 v187, 0xffff0000, v176
	v_lshlrev_b32_e32 v176, 16, v177
	v_and_b32_e32 v177, 0xffff0000, v177
	v_lshlrev_b32_e32 v188, 16, v178
	v_and_b32_e32 v189, 0xffff0000, v178
	v_lshlrev_b32_e32 v178, 16, v179
	v_and_b32_e32 v179, 0xffff0000, v179
	v_pk_add_f32 v[128:129], v[128:129], v[172:173]
	v_pk_add_f32 v[126:127], v[126:127], v[182:183]
	v_pk_add_f32 v[124:125], v[124:125], v[174:175]
	v_pk_add_f32 v[122:123], v[122:123], v[184:185]
	v_pk_add_f32 v[120:121], v[120:121], v[176:177]
	v_pk_add_f32 v[118:119], v[118:119], v[186:187]
	v_pk_add_f32 v[172:173], v[116:117], v[178:179]
	v_pk_add_f32 v[174:175], v[114:115], v[188:189]
	v_cmp_gt_u32_e32 vcc, 16, v171
	v_cvt_pk_bf16_f32 v114, v126, v127
	v_cvt_pk_bf16_f32 v115, v128, v129
	v_mul_f32_e32 v116, v127, v127
	v_mul_f32_e32 v117, v129, v129
	v_mul_f32_e32 v127, v123, v123
	v_mul_f32_e32 v129, v125, v125
	v_mul_f32_e32 v171, v119, v119
	v_mul_f32_e32 v176, v121, v121
	v_mul_f32_e32 v177, v175, v175
	v_mul_f32_e32 v178, v173, v173
	v_fmac_f32_e32 v116, v126, v126
	v_fmac_f32_e32 v117, v128, v128
	v_fmac_f32_e32 v127, v122, v122
	v_fmac_f32_e32 v129, v124, v124
	v_fmac_f32_e32 v171, v118, v118
	v_fmac_f32_e32 v176, v120, v120
	v_fmac_f32_e32 v177, v174, v174
	v_fmac_f32_e32 v178, v172, v172
	v_add_f32_e32 v116, v116, v117
	v_add_f32_e32 v117, v127, v129
	v_add_f32_e32 v126, v171, v176
	v_add_f32_e32 v127, v177, v178
	v_add_f32_e32 v116, v116, v117
	v_add_f32_e32 v117, v126, v127
	v_add_f32_e32 v126, v116, v117
	ds_bpermute_b32 v127, v170, v126
	v_cvt_pk_bf16_f32 v116, v122, v123
	v_cvt_pk_bf16_f32 v117, v124, v125
	flat_store_dwordx4 v[180:181], v[114:117]
	s_waitcnt lgkmcnt(0)
	s_nop 0
	v_add_f32_e32 v114, v126, v127
	ds_bpermute_b32 v115, v167, v114
	v_cvt_pk_bf16_f32 v116, v118, v119
	v_cvt_pk_bf16_f32 v117, v120, v121
	v_cvt_pk_bf16_f32 v118, v174, v175
	v_cvt_pk_bf16_f32 v119, v172, v173
	flat_store_dwordx4 v[180:181], v[116:119] offset:256
	s_and_saveexec_b64 s[18:19], vcc
	s_cbranch_execz .LBB0_1091
	s_waitcnt lgkmcnt(0)
	v_add_f32_e32 v114, v114, v115
	v_mul_f32_e32 v114, 0x4b800000, v114
	v_trunc_f32_e32 v114, v114
	v_mul_f32_e32 v115, 0x2f800000, v114
	v_floor_f32_e32 v115, v115
	v_fmac_f32_e32 v114, 0xcf800000, v115
	v_cvt_u32_f32_e32 v114, v114
	v_cvt_u32_f32_e32 v115, v115
	v_lshl_add_u64 v[116:117], v[156:157], 3, s[8:9]
	flat_atomic_add_x2 v[116:117], v[114:115]

; __device__ __forceinline__ u64_t ssq_fix(float ss) { return (u64_t)(ss * 16777216.0f); }
; #define ROW_FENCE() asm volatile("" ::: "memory")
; __device__ __forceinline__ u32x4 pack8(const f32x4& a, const f32x4& b) { u32x4 w; w.x = pk_bf16(a[0], a[1]); w.y = pk_bf16(a[2], a[3]); w.z = pk_bf16(b[0], b[1]); w.w = pk_bf16(b[2], b[3]); return w; }
; __device__ __forceinline__ void unpack8(const u32x4& w, f32x4& a, f32x4& b) { a = (f32x4){bf_lo(w.x), bf_hi(w.x), bf_lo(w.y), bf_hi(w.y)}; b = (f32x4){bf_lo(w.z), bf_hi(w.z), bf_lo(w.w), bf_hi(w.w)}; }
;     __device__ __forceinline__ void operator()(const f32x4 (&acc)[2][2][4][2], const pg8::Unit& u, int wr, int wc, int fr, int fq) const {
;     ...
;         for (int ai = 0; ai < 2; ++ai) {
;             u32x4 bs[4][2];
; #pragma unroll
;             for (int m = 0; m < 4; ++m) { const size_t off = (size_t)(u.pm * 256 + ai * 128 + wr * 64 + m * 16 + fr) * D + col;
; #pragma unroll
;                 for (int bj = 0; bj < 2; ++bj) bs[m][bj] = *(const u32x4*)(xb + off + bj * 128); }
;             ROW_FENCE();
; #pragma unroll
;             for (int m = 0; m < 4; ++m) {
;                 const int row = u.pm * 256 + ai * 128 + wr * 64 + m * 16 + fr; const size_t off = (size_t)row * D + col; float ss = 0.f;
;                 float rsc = osc; if constexpr (SC) asm volatile("" : "+v"(rsc));
; #pragma unroll
;                 for (int bj = 0; bj < 2; ++bj) { f32x4 b0, b1; unpack8(bs[m][bj], b0, b1); const f32x4 x0 = SC ? b0 + acc[ai][bj][m][0] * rsc : b0 + acc[ai][bj][m][0], x1 = SC ? b1 + acc[ai][bj][m][1] * rsc : b1 + acc[ai][bj][m][1];
;                     if (!dry) *(u32x4*)(xb + off + bj * 128) = pack8(x0, x1);
;                     ss += ((x0[0] * x0[0] + x0[1] * x0[1]) + (x0[2] * x0[2] + x0[3] * x0[3])) + ((x1[0] * x1[0] + x1[1] * x1[1]) + (x1[2] * x1[2] + x1[3] * x1[3])); }
;                 ss += __shfl_xor(ss, 16); ss += __shfl_xor(ss, 32);
;                 if (fq == 0 && !dry) atomicAdd(ssq + row, ssq_fix(ss));
;             }
.LBB0_1097:
	s_or_b64 exec, exec, s[18:19]
	v_add_u32_e32 v64, 0x80, v156
	s_waitcnt lgkmcnt(0)
	v_ashrrev_i32_e32 v65, 31, v64
	v_lshlrev_b64 v[64:65], 11, v[64:65]
	v_lshl_add_u64 v[94:95], v[158:159], 0, v[64:65]
	v_mov_b64_e32 v[96:97], v[206:207]
	v_mov_b64_e32 v[98:99], v[208:209]
	v_mov_b64_e32 v[100:101], v[210:211]
	v_mov_b64_e32 v[102:103], v[212:213]
	v_add_u32_e32 v64, 0x90, v156
	v_ashrrev_i32_e32 v65, 31, v64
	v_lshlrev_b64 v[64:65], 11, v[64:65]
	v_lshl_add_u64 v[92:93], v[158:159], 0, v[64:65]
	v_add_u32_e32 v64, 0xa0, v156
	v_ashrrev_i32_e32 v65, 31, v64
	v_lshlrev_b64 v[64:65], 11, v[64:65]
	v_lshl_add_u64 v[90:91], v[158:159], 0, v[64:65]
	v_add_u32_e32 v64, 0xb0, v156
	v_ashrrev_i32_e32 v65, 31, v64
	v_lshlrev_b64 v[64:65], 11, v[64:65]
	v_lshl_add_u64 v[88:89], v[158:159], 0, v[64:65]
	v_mov_b64_e32 v[84:85], v[214:215]
	v_mov_b64_e32 v[86:87], v[216:217]
	v_mov_b64_e32 v[80:81], v[218:219]
	v_mov_b64_e32 v[82:83], v[220:221]
	v_mov_b64_e32 v[76:77], v[222:223]
	v_mov_b64_e32 v[78:79], v[224:225]
	v_mov_b64_e32 v[72:73], v[226:227]
	v_mov_b64_e32 v[74:75], v[228:229]
	v_mov_b64_e32 v[68:69], v[230:231]
	v_mov_b64_e32 v[70:71], v[232:233]
	v_mov_b64_e32 v[64:65], v[234:235]
	v_mov_b64_e32 v[66:67], v[236:237]
	s_waitcnt vmcnt(0) lgkmcnt(0)
	v_lshlrev_b32_e32 v104, 16, v96
	v_and_b32_e32 v105, 0xffff0000, v96
	v_lshlrev_b32_e32 v96, 16, v97
	v_and_b32_e32 v97, 0xffff0000, v97
	v_lshlrev_b32_e32 v106, 16, v98
	v_and_b32_e32 v107, 0xffff0000, v98
	v_lshlrev_b32_e32 v98, 16, v99
	v_and_b32_e32 v99, 0xffff0000, v99
	v_pk_add_f32 v[62:63], v[62:63], v[96:97]
	v_pk_add_f32 v[60:61], v[60:61], v[104:105]
	v_pk_add_f32 v[96:97], v[58:59], v[98:99]
	v_pk_add_f32 v[98:99], v[56:57], v[106:107]
	v_cvt_pk_bf16_f32 v56, v60, v61
	v_cvt_pk_bf16_f32 v57, v62, v63
	v_cvt_pk_bf16_f32 v58, v98, v99
	v_cvt_pk_bf16_f32 v59, v96, v97
	flat_store_dwordx4 v[94:95], v[56:59]
	s_nop 1
	v_mul_f32_e32 v56, v61, v61
	v_mul_f32_e32 v57, v63, v63
	v_fmac_f32_e32 v56, v60, v60
	v_fmac_f32_e32 v57, v62, v62
	v_add_f32_e32 v56, v56, v57
	v_mul_f32_e32 v57, v99, v99
	v_mul_f32_e32 v58, v97, v97
	v_fmac_f32_e32 v57, v98, v98
	v_fmac_f32_e32 v58, v96, v96
	v_add_f32_e32 v57, v57, v58
	v_add_f32_e32 v96, v56, v57
	v_lshlrev_b32_e32 v56, 16, v100
	v_and_b32_e32 v57, 0xffff0000, v100
	v_lshlrev_b32_e32 v58, 16, v101
	v_and_b32_e32 v59, 0xffff0000, v101
	v_lshlrev_b32_e32 v60, 16, v102
	v_and_b32_e32 v61, 0xffff0000, v102
	v_lshlrev_b32_e32 v62, 16, v103
	v_and_b32_e32 v63, 0xffff0000, v103
	v_pk_add_f32 v[54:55], v[54:55], v[58:59]
	v_pk_add_f32 v[52:53], v[52:53], v[56:57]
	v_pk_add_f32 v[56:57], v[50:51], v[62:63]
	v_pk_add_f32 v[58:59], v[48:49], v[60:61]
	v_cvt_pk_bf16_f32 v48, v52, v53
	v_cvt_pk_bf16_f32 v49, v54, v55
	v_cvt_pk_bf16_f32 v50, v58, v59
	v_cvt_pk_bf16_f32 v51, v56, v57
	flat_store_dwordx4 v[94:95], v[48:51] offset:256
	s_nop 1
	v_mul_f32_e32 v48, v53, v53
	v_mul_f32_e32 v49, v55, v55
	v_fmac_f32_e32 v48, v52, v52
	v_fmac_f32_e32 v49, v54, v54
	v_add_f32_e32 v48, v48, v49
	v_mul_f32_e32 v49, v59, v59
	v_mul_f32_e32 v50, v57, v57
	v_fmac_f32_e32 v49, v58, v58
	v_fmac_f32_e32 v50, v56, v56
	v_add_f32_e32 v49, v49, v50
	v_add_f32_e32 v48, v48, v49
	v_add_f32_e32 v48, v96, v48
	ds_bpermute_b32 v49, v170, v48
	s_waitcnt lgkmcnt(0)
	v_add_f32_e32 v48, v48, v49
	ds_bpermute_b32 v49, v167, v48
	s_and_saveexec_b64 s[18:19], vcc
	s_cbranch_execz .LBB0_1099
	s_waitcnt lgkmcnt(0)
	v_add_f32_e32 v48, v48, v49
	v_mul_f32_e32 v48, 0x4b800000, v48
	v_trunc_f32_e32 v48, v48
	v_mul_f32_e32 v49, 0x2f800000, v48
	v_floor_f32_e32 v49, v49
	v_fmac_f32_e32 v48, 0xcf800000, v49
	v_cvt_u32_f32_e32 v48, v48
	v_cvt_u32_f32_e32 v49, v49
	v_lshl_add_u64 v[50:51], v[156:157], 3, s[8:9]
	flat_atomic_add_x2 v[50:51], v[48:49] offset:1024

; __device__ __forceinline__ u64_t* ssq_ptr(unsigned char* ws, int v) { return (u64_t*)(ws + CTL_SSQ) + (size_t)v * NTOK; }
; __device__ __forceinline__ u64_t ssq_fix(float ss) { return (u64_t)(ss * 16777216.0f); }
; #define ROW_FENCE() asm volatile("" ::: "memory")
; __device__ __forceinline__ u32x4 pack8(const f32x4& a, const f32x4& b) { u32x4 w; w.x = pk_bf16(a[0], a[1]); w.y = pk_bf16(a[2], a[3]); w.z = pk_bf16(b[0], b[1]); w.w = pk_bf16(b[2], b[3]); return w; }
;     __device__ __forceinline__ void operator()(const f32x4 (&acc)[2][2][4][2], const pg8::Unit& u, int wr, int wc, int fr, int fq) const {
;         bf16_t* xb = (bf16_t*)(ws + WS_XB); u64_t* ssq = ssq_ptr(ws, v);
;         float osc = 1.0f; if constexpr (SC) osc = __uint_as_float(((const unsigned*)(ws + CTL_AMAX))[AMAX_W2]) * (1.0f / 256.0f);
;         const int col = u.pn * 256 + wc * 32 + 8 * fq;
; #pragma unroll
;         for (int ai = 0; ai < 2; ++ai) {
;             u32x4 bs[4][2];
; #pragma unroll
;             for (int m = 0; m < 4; ++m) { const size_t off = (size_t)(u.pm * 256 + ai * 128 + wr * 64 + m * 16 + fr) * D + col;
; #pragma unroll
;                 for (int bj = 0; bj < 2; ++bj) bs[m][bj] = *(const u32x4*)(xb + off + bj * 128); }
;             ROW_FENCE();
; #pragma unroll
;             for (int m = 0; m < 4; ++m) {
;                 const int row = u.pm * 256 + ai * 128 + wr * 64 + m * 16 + fr; const size_t off = (size_t)row * D + col; float ss = 0.f;
;                 float rsc = osc; if constexpr (SC) asm volatile("" : "+v"(rsc));
; #pragma unroll
;                 for (int bj = 0; bj < 2; ++bj) { f32x4 b0, b1; unpack8(bs[m][bj], b0, b1); const f32x4 x0 = SC ? b0 + acc[ai][bj][m][0] * rsc : b0 + acc[ai][bj][m][0], x1 = SC ? b1 + acc[ai][bj][m][1] * rsc : b1 + acc[ai][bj][m][1];
;                     if (!dry) *(u32x4*)(xb + off + bj * 128) = pack8(x0, x1);
;                     ss += ((x0[0] * x0[0] + x0[1] * x0[1]) + (x0[2] * x0[2] + x0[3] * x0[3])) + ((x1[0] * x1[0] + x1[1] * x1[1]) + (x1[2] * x1[2] + x1[3] * x1[3])); }
;                 ss += __shfl_xor(ss, 16); ss += __shfl_xor(ss, 32);
;                 if (fq == 0 && !dry) atomicAdd(ssq + row, ssq_fix(ss));
;             }
.LBB0_1840:
	s_mov_b32 s2, s93
	s_nop 0
	v_mbcnt_lo_u32_b32 v130, -1, s2
	v_mbcnt_hi_u32_b32 v132, -1, v130
	v_mov_b64_e32 v[130:131], s[12:13]
	flat_load_dword v130, v[130:131]
	s_lshl_b32 s2, s44, 8
	s_or_b32 s2, s2, s36
	v_cmp_gt_u32_e32 vcc, 16, v132
	s_waitcnt vmcnt(0) lgkmcnt(0)
	v_mul_f32_e32 v158, 0x3b800000, v130
	v_ashrrev_i32_e32 v130, 1, v132
	v_and_b32_e32 v130, -8, v130
	v_add_u32_e32 v130, s2, v130
	s_lshl_b32 s2, s43, 8
	s_add_i32 s2, s2, s35
	v_and_or_b32 v156, v132, 15, s2
	v_ashrrev_i32_e32 v131, 31, v130
	v_ashrrev_i32_e32 v157, 31, v156
	v_lshl_add_u64 v[160:161], v[130:131], 1, s[8:9]
	v_lshlrev_b64 v[130:131], 11, v[156:157]
	v_lshl_add_u64 v[166:167], v[160:161], 0, v[130:131]
	flat_load_dwordx4 v[172:175], v[166:167]
	flat_load_dwordx4 v[176:179], v[166:167] offset:256
	v_or_b32_e32 v130, 16, v156
	v_ashrrev_i32_e32 v131, 31, v130
	v_lshlrev_b64 v[130:131], 11, v[130:131]
	v_lshl_add_u64 v[170:171], v[160:161], 0, v[130:131]
	v_or_b32_e32 v130, 32, v156
	v_ashrrev_i32_e32 v131, 31, v130
	v_lshlrev_b64 v[130:131], 11, v[130:131]
	v_lshl_add_u64 v[168:169], v[160:161], 0, v[130:131]
	v_or_b32_e32 v130, 48, v156
	v_ashrrev_i32_e32 v131, 31, v130
	v_lshlrev_b64 v[130:131], 11, v[130:131]
	v_lshl_add_u64 v[162:163], v[160:161], 0, v[130:131]
	flat_load_dwordx4 v[150:153], v[170:171]
	flat_load_dwordx4 v[146:149], v[170:171] offset:256
	flat_load_dwordx4 v[142:145], v[168:169]
	flat_load_dwordx4 v[138:141], v[168:169] offset:256
	flat_load_dwordx4 v[134:137], v[162:163]
	flat_load_dwordx4 v[130:133], v[162:163] offset:256
	v_mov_b32_e32 v246, 0x40000
	v_mov_b32_e32 v247, 0
	v_lshl_add_u64 v[238:239], v[166:167], 0, v[246:247]
	v_lshl_add_u64 v[240:241], v[170:171], 0, v[246:247]
	v_lshl_add_u64 v[242:243], v[168:169], 0, v[246:247]
	v_lshl_add_u64 v[244:245], v[162:163], 0, v[246:247]
	flat_load_dwordx4 v[206:209], v[238:239]
	flat_load_dwordx4 v[210:213], v[238:239] offset:256
	flat_load_dwordx4 v[214:217], v[240:241]
	flat_load_dwordx4 v[218:221], v[240:241] offset:256
	flat_load_dwordx4 v[222:225], v[242:243]
	flat_load_dwordx4 v[226:229], v[242:243] offset:256
	flat_load_dwordx4 v[230:233], v[244:245]
	flat_load_dwordx4 v[234:237], v[244:245] offset:256
	v_mov_b32_e32 v180, v158
	s_waitcnt vmcnt(0) lgkmcnt(0)
	v_lshlrev_b32_e32 v182, 16, v172
	v_and_b32_e32 v183, 0xffff0000, v172
	v_lshlrev_b32_e32 v172, 16, v173
	v_and_b32_e32 v173, 0xffff0000, v173
	v_lshlrev_b32_e32 v184, 16, v174
	v_and_b32_e32 v185, 0xffff0000, v174
	v_lshlrev_b32_e32 v174, 16, v175
	v_and_b32_e32 v175, 0xffff0000, v175
	v_pk_fma_f32 v[128:129], v[128:129], v[180:181], v[172:173] op_sel_hi:[1,0,1]
	v_pk_fma_f32 v[126:127], v[126:127], v[180:181], v[182:183] op_sel_hi:[1,0,1]
	v_pk_fma_f32 v[172:173], v[124:125], v[180:181], v[174:175] op_sel_hi:[1,0,1]
	v_pk_fma_f32 v[174:175], v[122:123], v[180:181], v[184:185] op_sel_hi:[1,0,1]
	v_cvt_pk_bf16_f32 v122, v126, v127
	v_cvt_pk_bf16_f32 v123, v128, v129
	v_cvt_pk_bf16_f32 v124, v174, v175
	v_cvt_pk_bf16_f32 v125, v172, v173
	flat_store_dwordx4 v[166:167], v[122:125]
	s_nop 1
	v_mul_f32_e32 v122, v127, v127
	v_mul_f32_e32 v123, v129, v129
	v_fmac_f32_e32 v122, v126, v126
	v_fmac_f32_e32 v123, v128, v128
	v_add_f32_e32 v122, v122, v123
	v_mul_f32_e32 v123, v175, v175
	v_mul_f32_e32 v124, v173, v173
	v_fmac_f32_e32 v123, v174, v174
	v_fmac_f32_e32 v124, v172, v172
	v_add_f32_e32 v123, v123, v124
	v_add_f32_e32 v172, v122, v123
	v_lshlrev_b32_e32 v122, 16, v176
	v_and_b32_e32 v123, 0xffff0000, v176
	v_lshlrev_b32_e32 v124, 16, v177
	v_and_b32_e32 v125, 0xffff0000, v177
	v_lshlrev_b32_e32 v126, 16, v178
	v_and_b32_e32 v127, 0xffff0000, v178
	v_lshlrev_b32_e32 v128, 16, v179
	v_and_b32_e32 v129, 0xffff0000, v179
	v_pk_fma_f32 v[120:121], v[120:121], v[180:181], v[124:125] op_sel_hi:[1,0,1]
	v_pk_fma_f32 v[118:119], v[118:119], v[180:181], v[122:123] op_sel_hi:[1,0,1]
	v_pk_fma_f32 v[122:123], v[116:117], v[180:181], v[128:129] op_sel_hi:[1,0,1]
	v_pk_fma_f32 v[124:125], v[114:115], v[180:181], v[126:127] op_sel_hi:[1,0,1]
	v_cvt_pk_bf16_f32 v114, v118, v119
	v_cvt_pk_bf16_f32 v115, v120, v121
	v_cvt_pk_bf16_f32 v116, v124, v125
	v_cvt_pk_bf16_f32 v117, v122, v123
	flat_store_dwordx4 v[166:167], v[114:117] offset:256
	s_nop 1
	v_mul_f32_e32 v114, v119, v119
	v_mul_f32_e32 v115, v121, v121
	v_fmac_f32_e32 v114, v118, v118
	v_fmac_f32_e32 v115, v120, v120
	v_add_f32_e32 v114, v114, v115
	v_mul_f32_e32 v115, v125, v125
	v_mul_f32_e32 v116, v123, v123
	v_fmac_f32_e32 v115, v124, v124
	v_fmac_f32_e32 v116, v122, v122
	v_add_f32_e32 v115, v115, v116
	v_add_f32_e32 v114, v114, v115
	v_and_b32_e32 v116, 64, v251
	v_add_f32_e32 v115, v172, v114
	v_xor_b32_e32 v114, 16, v251
	v_add_u32_e32 v117, 64, v116
	v_cmp_lt_i32_e64 s[2:3], v114, v117
	s_nop 1
	v_cndmask_b32_e64 v114, v251, v114, s[2:3]
	v_lshlrev_b32_e32 v114, 2, v114
	ds_bpermute_b32 v116, v114, v115
	s_waitcnt lgkmcnt(0)
	v_add_f32_e32 v116, v115, v116
	v_xor_b32_e32 v115, 32, v251
	v_cmp_lt_i32_e64 s[2:3], v115, v117
	s_nop 1
	v_cndmask_b32_e64 v115, v251, v115, s[2:3]
	v_lshlrev_b32_e32 v115, 2, v115
	ds_bpermute_b32 v117, v115, v116
	s_and_saveexec_b64 s[2:3], vcc
	s_cbranch_execz .LBB0_1842
	s_waitcnt lgkmcnt(0)
	v_add_f32_e32 v116, v116, v117
	v_mul_f32_e32 v116, 0x4b800000, v116
	v_trunc_f32_e32 v116, v116
	v_mul_f32_e32 v117, 0x2f800000, v116
	v_floor_f32_e32 v117, v117
	v_fmac_f32_e32 v116, 0xcf800000, v117
	v_cvt_u32_f32_e32 v116, v116
	v_cvt_u32_f32_e32 v117, v117
	v_lshl_add_u64 v[118:119], v[156:157], 3, s[10:11]
	flat_atomic_add_x2 v[118:119], v[116:117]

; __device__ __forceinline__ u64_t ssq_fix(float ss) { return (u64_t)(ss * 16777216.0f); }
; #define ROW_FENCE() asm volatile("" ::: "memory")
; __device__ __forceinline__ u32x4 pack8(const f32x4& a, const f32x4& b) { u32x4 w; w.x = pk_bf16(a[0], a[1]); w.y = pk_bf16(a[2], a[3]); w.z = pk_bf16(b[0], b[1]); w.w = pk_bf16(b[2], b[3]); return w; }
; __device__ __forceinline__ void unpack8(const u32x4& w, f32x4& a, f32x4& b) { a = (f32x4){bf_lo(w.x), bf_hi(w.x), bf_lo(w.y), bf_hi(w.y)}; b = (f32x4){bf_lo(w.z), bf_hi(w.z), bf_lo(w.w), bf_hi(w.w)}; }
;     __device__ __forceinline__ void operator()(const f32x4 (&acc)[2][2][4][2], const pg8::Unit& u, int wr, int wc, int fr, int fq) const {
;     ...
;         for (int ai = 0; ai < 2; ++ai) {
;             u32x4 bs[4][2];
; #pragma unroll
;             for (int m = 0; m < 4; ++m) { const size_t off = (size_t)(u.pm * 256 + ai * 128 + wr * 64 + m * 16 + fr) * D + col;
; #pragma unroll
;                 for (int bj = 0; bj < 2; ++bj) bs[m][bj] = *(const u32x4*)(xb + off + bj * 128); }
;             ROW_FENCE();
; #pragma unroll
;             for (int m = 0; m < 4; ++m) {
;                 const int row = u.pm * 256 + ai * 128 + wr * 64 + m * 16 + fr; const size_t off = (size_t)row * D + col; float ss = 0.f;
;                 float rsc = osc; if constexpr (SC) asm volatile("" : "+v"(rsc));
; #pragma unroll
;                 for (int bj = 0; bj < 2; ++bj) { f32x4 b0, b1; unpack8(bs[m][bj], b0, b1); const f32x4 x0 = SC ? b0 + acc[ai][bj][m][0] * rsc : b0 + acc[ai][bj][m][0], x1 = SC ? b1 + acc[ai][bj][m][1] * rsc : b1 + acc[ai][bj][m][1];
;                     if (!dry) *(u32x4*)(xb + off + bj * 128) = pack8(x0, x1);
;                     ss += ((x0[0] * x0[0] + x0[1] * x0[1]) + (x0[2] * x0[2] + x0[3] * x0[3])) + ((x1[0] * x1[0] + x1[1] * x1[1]) + (x1[2] * x1[2] + x1[3] * x1[3])); }
;                 ss += __shfl_xor(ss, 16); ss += __shfl_xor(ss, 32);
;                 if (fq == 0 && !dry) atomicAdd(ssq + row, ssq_fix(ss));
;             }
.LBB0_1848:
	s_or_b64 exec, exec, s[2:3]
	v_add_u32_e32 v64, 0x80, v156
	s_waitcnt lgkmcnt(0)
	v_ashrrev_i32_e32 v65, 31, v64
	v_lshlrev_b64 v[64:65], 11, v[64:65]
	v_lshl_add_u64 v[98:99], v[160:161], 0, v[64:65]
	v_mov_b64_e32 v[100:101], v[206:207]
	v_mov_b64_e32 v[102:103], v[208:209]
	v_mov_b64_e32 v[88:89], v[210:211]
	v_mov_b64_e32 v[90:91], v[212:213]
	v_add_u32_e32 v64, 0x90, v156
	v_ashrrev_i32_e32 v65, 31, v64
	v_lshlrev_b64 v[64:65], 11, v[64:65]
	v_lshl_add_u64 v[96:97], v[160:161], 0, v[64:65]
	v_add_u32_e32 v64, 0xa0, v156
	v_ashrrev_i32_e32 v65, 31, v64
	v_lshlrev_b64 v[64:65], 11, v[64:65]
	v_lshl_add_u64 v[94:95], v[160:161], 0, v[64:65]
	v_add_u32_e32 v64, 0xb0, v156
	v_ashrrev_i32_e32 v65, 31, v64
	v_lshlrev_b64 v[64:65], 11, v[64:65]
	v_lshl_add_u64 v[92:93], v[160:161], 0, v[64:65]
	v_mov_b64_e32 v[84:85], v[214:215]
	v_mov_b64_e32 v[86:87], v[216:217]
	v_mov_b64_e32 v[80:81], v[218:219]
	v_mov_b64_e32 v[82:83], v[220:221]
	v_mov_b64_e32 v[76:77], v[222:223]
	v_mov_b64_e32 v[78:79], v[224:225]
	v_mov_b64_e32 v[72:73], v[226:227]
	v_mov_b64_e32 v[74:75], v[228:229]
	v_mov_b64_e32 v[68:69], v[230:231]
	v_mov_b64_e32 v[70:71], v[232:233]
	v_mov_b64_e32 v[64:65], v[234:235]
	v_mov_b64_e32 v[66:67], v[236:237]
	v_mov_b32_e32 v104, v158
	s_waitcnt vmcnt(0) lgkmcnt(0)
	v_lshlrev_b32_e32 v106, 16, v100
	v_and_b32_e32 v107, 0xffff0000, v100
	v_lshlrev_b32_e32 v100, 16, v101
	v_and_b32_e32 v101, 0xffff0000, v101
	v_lshlrev_b32_e32 v108, 16, v102
	v_and_b32_e32 v109, 0xffff0000, v102
	v_lshlrev_b32_e32 v102, 16, v103
	v_and_b32_e32 v103, 0xffff0000, v103
	v_pk_fma_f32 v[62:63], v[62:63], v[104:105], v[100:101] op_sel_hi:[1,0,1]
	v_pk_fma_f32 v[60:61], v[60:61], v[104:105], v[106:107] op_sel_hi:[1,0,1]
	v_pk_fma_f32 v[100:101], v[58:59], v[104:105], v[102:103] op_sel_hi:[1,0,1]
	v_pk_fma_f32 v[102:103], v[56:57], v[104:105], v[108:109] op_sel_hi:[1,0,1]
	v_cvt_pk_bf16_f32 v56, v60, v61
	v_cvt_pk_bf16_f32 v57, v62, v63
	v_cvt_pk_bf16_f32 v58, v102, v103
	v_cvt_pk_bf16_f32 v59, v100, v101
	flat_store_dwordx4 v[98:99], v[56:59]
	s_nop 1
	v_mul_f32_e32 v56, v61, v61
	v_mul_f32_e32 v57, v63, v63
	v_fmac_f32_e32 v56, v60, v60
	v_fmac_f32_e32 v57, v62, v62
	v_add_f32_e32 v56, v56, v57
	v_mul_f32_e32 v57, v103, v103
	v_mul_f32_e32 v58, v101, v101
	v_fmac_f32_e32 v57, v102, v102
	v_fmac_f32_e32 v58, v100, v100
	v_add_f32_e32 v57, v57, v58
	v_add_f32_e32 v100, v56, v57
	v_lshlrev_b32_e32 v56, 16, v88
	v_and_b32_e32 v57, 0xffff0000, v88
	v_lshlrev_b32_e32 v58, 16, v89
	v_and_b32_e32 v59, 0xffff0000, v89
	v_lshlrev_b32_e32 v60, 16, v90
	v_and_b32_e32 v61, 0xffff0000, v90
	v_lshlrev_b32_e32 v62, 16, v91
	v_and_b32_e32 v63, 0xffff0000, v91
	v_pk_fma_f32 v[54:55], v[54:55], v[104:105], v[58:59] op_sel_hi:[1,0,1]
	v_pk_fma_f32 v[52:53], v[52:53], v[104:105], v[56:57] op_sel_hi:[1,0,1]
	v_pk_fma_f32 v[56:57], v[50:51], v[104:105], v[62:63] op_sel_hi:[1,0,1]
	v_pk_fma_f32 v[58:59], v[48:49], v[104:105], v[60:61] op_sel_hi:[1,0,1]
	v_cvt_pk_bf16_f32 v48, v52, v53
	v_cvt_pk_bf16_f32 v49, v54, v55
	v_cvt_pk_bf16_f32 v50, v58, v59
	v_cvt_pk_bf16_f32 v51, v56, v57
	flat_store_dwordx4 v[98:99], v[48:51] offset:256
	s_nop 1
	v_mul_f32_e32 v48, v53, v53
	v_mul_f32_e32 v49, v55, v55
	v_fmac_f32_e32 v48, v52, v52
	v_fmac_f32_e32 v49, v54, v54
	v_add_f32_e32 v48, v48, v49
	v_mul_f32_e32 v49, v59, v59
	v_mul_f32_e32 v50, v57, v57
	v_fmac_f32_e32 v49, v58, v58
	v_fmac_f32_e32 v50, v56, v56
	v_add_f32_e32 v49, v49, v50
	v_add_f32_e32 v48, v48, v49
	v_add_f32_e32 v48, v100, v48
	ds_bpermute_b32 v49, v114, v48
	s_waitcnt lgkmcnt(0)
	v_add_f32_e32 v48, v48, v49
	ds_bpermute_b32 v49, v115, v48
	s_and_saveexec_b64 s[2:3], vcc
	s_cbranch_execz .LBB0_1850
	s_waitcnt lgkmcnt(0)
	v_add_f32_e32 v48, v48, v49
	v_mul_f32_e32 v48, 0x4b800000, v48
	v_trunc_f32_e32 v48, v48
	v_mul_f32_e32 v49, 0x2f800000, v48
	v_floor_f32_e32 v49, v49
	v_fmac_f32_e32 v48, 0xcf800000, v49
	v_cvt_u32_f32_e32 v48, v48
	v_cvt_u32_f32_e32 v49, v49
	v_lshl_add_u64 v[50:51], v[156:157], 3, s[10:11]
	flat_atomic_add_x2 v[50:51], v[48:49] offset:1024
